# down-GEMM filler conversion paced (s_sleep 48 per tile) so the workgroups still running GEMM tiles are not starved of memory bandwidth
# speedup vs baseline: 1.0023x; 1.0007x over previous
.LBB0_1409:
	s_sleep 48
	s_movk_i32 s0, 0x6cf
	v_cmp_lt_i32_e32 vcc, s0, v3
	s_and_saveexec_b64 s[0:1], vcc
	s_xor_b64 s[0:1], exec, s[0:1]
	s_cbranch_execz .LBB0_1419
	s_movk_i32 s18, 0x84f
	v_cmp_lt_u32_e32 vcc, s18, v3
	s_and_saveexec_b64 s[18:19], vcc
	s_xor_b64 s[18:19], exec, s[18:19]
	s_cbranch_execz .LBB0_1416
	s_movk_i32 s20, 0x94f
	v_cmp_lt_u32_e32 vcc, s20, v3
	s_and_saveexec_b64 s[20:21], vcc
	s_xor_b64 s[20:21], exec, s[20:21]
	s_cbranch_execz .LBB0_1413
	v_and_b32_e32 v84, 0x3c0, v52
	v_and_b32_e32 v130, 0x7800000, v54
	v_add_u32_e32 v85, 0xffffdac0, v53
	s_movk_i32 s22, 0x7c0
	v_or_b32_e32 v13, v84, v9
	v_lshl_add_u64 v[10:11], s[6:7], 0, v[130:131]
	v_lshl_add_u64 v[46:47], s[8:9], 0, v[130:131]
	v_and_or_b32 v12, v85, s22, v48
	v_lshlrev_b32_e32 v130, 13, v13
	v_lshl_add_u64 v[10:11], v[10:11], 0, v[130:131]
	v_lshlrev_b32_e32 v130, 2, v12
	v_lshl_add_u64 v[76:77], v[10:11], 0, v[130:131]
	s_waitcnt lgkmcnt(0)
	v_add_co_u32_e32 v14, vcc, 0x8000, v76
	s_mov_b32 s22, 0x20000
	s_nop 0
	v_addc_co_u32_e32 v15, vcc, 0, v77, vcc
	v_add_co_u32_e32 v18, vcc, 0x10000, v76
	global_load_dwordx4 v[10:13], v[76:77], off
	s_nop 0
	global_load_dwordx4 v[14:17], v[14:15], off
	v_addc_co_u32_e32 v19, vcc, 0, v77, vcc
	v_add_co_u32_e32 v22, vcc, 0x18000, v76
	s_nop 1
	v_addc_co_u32_e32 v23, vcc, 0, v77, vcc
	v_add_co_u32_e32 v26, vcc, s22, v76
	s_mov_b32 s22, 0x40000
	s_nop 0
	v_addc_co_u32_e32 v27, vcc, 0, v77, vcc
	v_add_co_u32_e32 v30, vcc, 0x28000, v76
	global_load_dwordx4 v[18:21], v[18:19], off
	s_nop 0
	global_load_dwordx4 v[22:25], v[22:23], off
	v_addc_co_u32_e32 v31, vcc, 0, v77, vcc
	v_add_co_u32_e32 v34, vcc, 0x30000, v76
	global_load_dwordx4 v[26:29], v[26:27], off
	s_nop 0
	global_load_dwordx4 v[30:33], v[30:31], off
	v_addc_co_u32_e32 v35, vcc, 0, v77, vcc
	v_add_co_u32_e32 v38, vcc, 0x38000, v76
	s_nop 1
	v_addc_co_u32_e32 v39, vcc, 0, v77, vcc
	v_add_co_u32_e32 v42, vcc, s22, v76
	global_load_dwordx4 v[34:37], v[34:35], off
	s_nop 0
	global_load_dwordx4 v[38:41], v[38:39], off
	v_addc_co_u32_e32 v43, vcc, 0, v77, vcc
	v_add_co_u32_e32 v56, vcc, 0x48000, v76
	s_nop 1
	v_addc_co_u32_e32 v57, vcc, 0, v77, vcc
	v_add_co_u32_e32 v60, vcc, 0x50000, v76
	global_load_dwordx4 v[42:45], v[42:43], off
	s_nop 0
	global_load_dwordx4 v[56:59], v[56:57], off
	v_addc_co_u32_e32 v61, vcc, 0, v77, vcc
	v_add_co_u32_e32 v64, vcc, 0x58000, v76
	s_nop 1
	v_addc_co_u32_e32 v65, vcc, 0, v77, vcc
	v_add_co_u32_e32 v68, vcc, 0x60000, v76
	global_load_dwordx4 v[60:63], v[60:61], off
	s_nop 0
	global_load_dwordx4 v[64:67], v[64:65], off
	v_addc_co_u32_e32 v69, vcc, 0, v77, vcc
	v_add_co_u32_e32 v72, vcc, 0x68000, v76
	s_nop 1
	v_addc_co_u32_e32 v73, vcc, 0, v77, vcc
	v_add_co_u32_e32 v78, vcc, 0x70000, v76
	global_load_dwordx4 v[68:71], v[68:69], off
	s_nop 0
	global_load_dwordx4 v[72:75], v[72:73], off
	v_addc_co_u32_e32 v79, vcc, 0, v77, vcc
	v_add_co_u32_e32 v80, vcc, 0x78000, v76
	s_nop 1
	v_addc_co_u32_e32 v81, vcc, 0, v77, vcc
	global_load_dwordx4 v[76:79], v[78:79], off
	s_nop 0
	global_load_dwordx4 v[80:83], v[80:81], off
	s_waitcnt vmcnt(0)
	ds_write2_b32 v49, v10, v11 offset1:1
	ds_write2_b32 v49, v12, v13 offset0:2 offset1:3
	v_add_u32_e32 v10, 0x410, v49
	ds_write2_b32 v10, v14, v15 offset1:1
	v_add_u32_e32 v10, 0x418, v49
	ds_write2_b32 v10, v16, v17 offset1:1
	v_add_u32_e32 v10, 0x820, v49
	ds_write2_b32 v10, v18, v19 offset1:1
	v_add_u32_e32 v10, 0x828, v49
	ds_write2_b32 v10, v20, v21 offset1:1
	v_add_u32_e32 v10, 0xc30, v49
	ds_write2_b32 v10, v22, v23 offset1:1
	v_add_u32_e32 v10, 0xc38, v49
	ds_write2_b32 v10, v24, v25 offset1:1
	v_add_u32_e32 v10, 0x1040, v49
	ds_write2_b32 v10, v26, v27 offset1:1
	v_add_u32_e32 v10, 0x1048, v49
	ds_write2_b32 v10, v28, v29 offset1:1
	v_add_u32_e32 v10, 0x1450, v49
	ds_write2_b32 v10, v30, v31 offset1:1
	v_add_u32_e32 v10, 0x1458, v49
	ds_write2_b32 v10, v32, v33 offset1:1
	v_add_u32_e32 v10, 0x1860, v49
	ds_write2_b32 v10, v34, v35 offset1:1
	v_add_u32_e32 v10, 0x1868, v49
	ds_write2_b32 v10, v36, v37 offset1:1
	v_add_u32_e32 v10, 0x1c70, v49
	ds_write2_b32 v10, v38, v39 offset1:1
	v_add_u32_e32 v10, 0x1c78, v49
	ds_write2_b32 v10, v40, v41 offset1:1
	v_add_u32_e32 v10, 0x2080, v49
	ds_write2_b32 v10, v42, v43 offset1:1
	v_add_u32_e32 v10, 0x2088, v49
	ds_write2_b32 v10, v44, v45 offset1:1
	v_add_u32_e32 v10, 0x2490, v49
	ds_write2_b32 v10, v56, v57 offset1:1
	v_add_u32_e32 v10, 0x2498, v49
	ds_write2_b32 v10, v58, v59 offset1:1
	v_add_u32_e32 v10, 0x28a0, v49
	ds_write2_b32 v10, v60, v61 offset1:1
	v_add_u32_e32 v10, 0x28a8, v49
	ds_write2_b32 v10, v62, v63 offset1:1
	v_add_u32_e32 v10, 0x2cb0, v49
	ds_write2_b32 v10, v64, v65 offset1:1
	v_add_u32_e32 v10, 0x2cb8, v49
	ds_write2_b32 v10, v66, v67 offset1:1
	v_add_u32_e32 v10, 0x30c0, v49
	ds_write2_b32 v10, v68, v69 offset1:1
	v_add_u32_e32 v10, 0x30c8, v49
	ds_write2_b32 v10, v70, v71 offset1:1
	v_add_u32_e32 v10, 0x34d0, v49
	ds_write2_b32 v10, v72, v73 offset1:1
	v_add_u32_e32 v10, 0x34d8, v49
	ds_write2_b32 v10, v74, v75 offset1:1
	v_add_u32_e32 v10, 0x38e0, v49
	ds_write2_b32 v10, v76, v77 offset1:1
	v_add_u32_e32 v10, 0x38e8, v49
	ds_write2_b32 v10, v78, v79 offset1:1
	v_add_u32_e32 v10, 0x3cf0, v49
	ds_write2_b32 v10, v80, v81 offset1:1
	v_add_u32_e32 v10, 0x3cf8, v49
	ds_write2_b32 v10, v82, v83 offset1:1
	v_add_u32_e32 v56, 0x400, v51
	ds_read2_b32 v[14:15], v51 offset0:65 offset1:73
	ds_read2_b32 v[16:17], v51 offset0:130 offset1:138
	ds_read2_b32 v[18:19], v51 offset0:195 offset1:203
	ds_read2_b32 v[20:21], v56 offset0:4 offset1:12
	ds_read2_b32 v[22:23], v56 offset0:69 offset1:77
	ds_read2_b32 v[24:25], v56 offset0:134 offset1:142
	ds_read2_b32 v[26:27], v56 offset0:199 offset1:207
	ds_read2_b32 v[28:29], v51 offset1:8
	ds_read2_b32 v[30:31], v51 offset0:16 offset1:24
	ds_read2_b32 v[32:33], v51 offset0:81 offset1:89
	ds_read2_b32 v[34:35], v51 offset0:146 offset1:154
	ds_read2_b32 v[36:37], v51 offset0:211 offset1:219
	ds_read2_b32 v[38:39], v56 offset0:20 offset1:28
	ds_read2_b32 v[40:41], v56 offset0:85 offset1:93
	ds_read2_b32 v[42:43], v56 offset0:150 offset1:158
	ds_read2_b32 v[44:45], v56 offset0:215 offset1:223
	v_lshlrev_b32_e32 v130, 1, v84
	v_lshl_add_u64 v[10:11], v[46:47], 0, v[130:131]
	v_lshlrev_b32_e32 v130, 1, v2
	v_lshl_add_u64 v[46:47], v[10:11], 0, v[130:131]
	v_lshlrev_b32_e32 v10, 1, v85
	v_and_b32_e32 v10, 0xf00, v10
	v_and_b32_e32 v11, 64, v85
	v_or3_b32 v57, v11, v10, v50
	v_lshlrev_b32_e32 v130, 11, v57
	v_lshl_add_u64 v[46:47], v[46:47], 0, v[130:131]
	s_waitcnt lgkmcnt(8)
	v_cvt_pk_bf16_f32 v10, v28, v14
	v_cvt_pk_bf16_f32 v11, v16, v18
	v_cvt_pk_bf16_f32 v12, v20, v22
	v_cvt_pk_bf16_f32 v13, v24, v26
	v_add_co_u32_e32 v14, vcc, s88, v46
	global_store_dwordx4 v[46:47], v[10:13], off
	s_nop 1
	v_cvt_pk_bf16_f32 v10, v29, v15
	v_cvt_pk_bf16_f32 v11, v17, v19
	v_cvt_pk_bf16_f32 v12, v21, v23
	v_cvt_pk_bf16_f32 v13, v25, v27
	v_addc_co_u32_e32 v15, vcc, 0, v47, vcc
	global_store_dwordx4 v[14:15], v[10:13], off
	v_add_co_u32_e32 v14, vcc, s77, v46
	s_waitcnt lgkmcnt(6)
	v_cvt_pk_bf16_f32 v10, v30, v32
	s_waitcnt lgkmcnt(4)
	v_cvt_pk_bf16_f32 v11, v34, v36
	s_waitcnt lgkmcnt(2)
	v_cvt_pk_bf16_f32 v12, v38, v40
	s_waitcnt lgkmcnt(0)
	v_cvt_pk_bf16_f32 v13, v42, v44
	v_addc_co_u32_e32 v15, vcc, 0, v47, vcc
	global_store_dwordx4 v[14:15], v[10:13], off
	v_add_co_u32_e32 v14, vcc, s82, v46
	s_nop 0
	v_cvt_pk_bf16_f32 v10, v31, v33
	v_cvt_pk_bf16_f32 v11, v35, v37
	v_cvt_pk_bf16_f32 v12, v39, v41
	v_cvt_pk_bf16_f32 v13, v43, v45
	v_addc_co_u32_e32 v15, vcc, 0, v47, vcc
	global_store_dwordx4 v[14:15], v[10:13], off
	ds_read2_b32 v[14:15], v51 offset0:97 offset1:105
	ds_read2_b32 v[16:17], v51 offset0:162 offset1:170
	ds_read2_b32 v[18:19], v51 offset0:227 offset1:235
	ds_read2_b32 v[20:21], v56 offset0:36 offset1:44
	ds_read2_b32 v[22:23], v56 offset0:101 offset1:109
	ds_read2_b32 v[24:25], v56 offset0:166 offset1:174
	ds_read2_b32 v[26:27], v56 offset0:231 offset1:239
	ds_read2_b32 v[28:29], v51 offset0:32 offset1:40
	ds_read2_b32 v[30:31], v51 offset0:48 offset1:56
	ds_read2_b32 v[32:33], v51 offset0:113 offset1:121
	ds_read2_b32 v[34:35], v51 offset0:178 offset1:186
	ds_read2_b32 v[36:37], v51 offset0:243 offset1:251
	ds_read2_b32 v[38:39], v56 offset0:52 offset1:60
	ds_read2_b32 v[40:41], v56 offset0:117 offset1:125
	ds_read2_b32 v[42:43], v56 offset0:182 offset1:190
	ds_read2_b32 v[44:45], v56 offset0:247 offset1:255
	v_add_co_u32_e32 v56, vcc, s80, v46
	s_mov_b32 s22, 0x14000
	s_nop 0
	v_addc_co_u32_e32 v57, vcc, 0, v47, vcc
	s_waitcnt lgkmcnt(8)
	v_cvt_pk_bf16_f32 v10, v28, v14
	v_cvt_pk_bf16_f32 v11, v16, v18
	v_cvt_pk_bf16_f32 v12, v20, v22
	v_cvt_pk_bf16_f32 v13, v24, v26
	v_add_co_u32_e32 v14, vcc, s22, v46
	global_store_dwordx4 v[56:57], v[10:13], off
	s_nop 1
	v_cvt_pk_bf16_f32 v10, v29, v15
	v_cvt_pk_bf16_f32 v11, v17, v19
	v_cvt_pk_bf16_f32 v12, v21, v23
	v_cvt_pk_bf16_f32 v13, v25, v27
	v_addc_co_u32_e32 v15, vcc, 0, v47, vcc
	global_store_dwordx4 v[14:15], v[10:13], off
	v_add_co_u32_e32 v14, vcc, s83, v46
	s_waitcnt lgkmcnt(6)
	v_cvt_pk_bf16_f32 v10, v30, v32
	s_waitcnt lgkmcnt(4)
	v_cvt_pk_bf16_f32 v11, v34, v36
	s_waitcnt lgkmcnt(2)
	v_cvt_pk_bf16_f32 v12, v38, v40
	s_waitcnt lgkmcnt(0)
	v_cvt_pk_bf16_f32 v13, v42, v44
	v_addc_co_u32_e32 v15, vcc, 0, v47, vcc
	global_store_dwordx4 v[14:15], v[10:13], off
	v_add_co_u32_e32 v14, vcc, 0x1c000, v46
	s_nop 0
	v_cvt_pk_bf16_f32 v10, v31, v33
	v_cvt_pk_bf16_f32 v11, v35, v37
	v_cvt_pk_bf16_f32 v12, v39, v41
	v_cvt_pk_bf16_f32 v13, v43, v45
	v_addc_co_u32_e32 v15, vcc, 0, v47, vcc
	global_store_dwordx4 v[14:15], v[10:13], off
